# l3x4
# speedup vs baseline: 1.1590x; 1.0020x over previous
.LBB0_44:
	v_lshl_or_b32 v7, s2, 8, v0
	v_and_b32_e32 v2, 31, v0
	v_bfe_u32 v3, v0, 5, 1
	s_cmp_lt_u32 s2, 12
	s_cbranch_scc1 .Lw1f8
	v_lshrrev_b32_e32 v1, 6, v7
	s_cmp_lt_u32 s2, 20
	v_readfirstlane_b32 s10, v1
	s_cbranch_scc1 .Lw2bf
	s_load_dwordx2 s[12:13], s[0:1], 0x20
	v_and_b32_e32 v2, 3, v0
	s_sub_u32 s10, s10, 0x50
	s_mul_i32 s10, s10, 0xc0
	v_mul_u32_u24_e32 v4, 48, v3
	v_lshl_add_u32 v4, v2, 2, v4
	v_add_u32_e32 v4, s10, v4
	v_add_u32_e32 v5, 0xffffec00, v7
	v_lshlrev_b32_e32 v5, 4, v5
	v_add_u32_e32 v5, 0x14000, v5
	v_mov_b32_e32 v16, 0
	v_mov_b32_e32 v17, 0
	v_mov_b32_e32 v18, 0
	v_mov_b32_e32 v19, 0
	v_mov_b32_e32 v20, 0
	v_mov_b32_e32 v21, 0
	v_mov_b32_e32 v22, 0
	v_mov_b32_e32 v23, 0
	v_cmp_gt_u32_e32 vcc, 3, v2
	s_and_saveexec_b64 s[14:15], vcc
	s_waitcnt lgkmcnt(0)
	global_load_dword v16, v4, s[12:13] offset:0
	global_load_dword v17, v4, s[12:13] offset:12
	global_load_dword v18, v4, s[12:13] offset:24
	global_load_dword v19, v4, s[12:13] offset:36
	global_load_dword v20, v4, s[12:13] offset:96
	global_load_dword v21, v4, s[12:13] offset:108
	global_load_dword v22, v4, s[12:13] offset:120
	global_load_dword v23, v4, s[12:13] offset:132
	s_or_b64 exec, exec, s[14:15]
	s_movk_i32 s16, 0x7fff
	s_mov_b32 s17, 0x7060302
	s_waitcnt vmcnt(7)
	v_mul_f32_e32 v16, 0x6f800000, v16
	v_bfe_u32 v24, v16, 16, 1
	s_waitcnt vmcnt(6)
	v_mul_f32_e32 v17, 0x6f800000, v17
	v_bfe_u32 v25, v17, 16, 1
	s_waitcnt vmcnt(5)
	v_mul_f32_e32 v18, 0x6f800000, v18
	v_bfe_u32 v26, v18, 16, 1
	s_waitcnt vmcnt(4)
	v_mul_f32_e32 v19, 0x6f800000, v19
	v_bfe_u32 v27, v19, 16, 1
	s_waitcnt vmcnt(3)
	v_mul_f32_e32 v20, 0x6f800000, v20
	v_bfe_u32 v28, v20, 16, 1
	s_waitcnt vmcnt(2)
	v_mul_f32_e32 v21, 0x6f800000, v21
	v_bfe_u32 v29, v21, 16, 1
	s_waitcnt vmcnt(1)
	v_mul_f32_e32 v22, 0x6f800000, v22
	v_bfe_u32 v30, v22, 16, 1
	s_waitcnt vmcnt(0)
	v_mul_f32_e32 v23, 0x6f800000, v23
	v_bfe_u32 v31, v23, 16, 1
	v_add3_u32 v16, v16, v24, s16
	v_add3_u32 v17, v17, v25, s16
	v_add3_u32 v18, v18, v26, s16
	v_add3_u32 v19, v19, v27, s16
	v_add3_u32 v20, v20, v28, s16
	v_add3_u32 v21, v21, v29, s16
	v_add3_u32 v22, v22, v30, s16
	v_add3_u32 v23, v23, v31, s16
	v_perm_b32 v0, v17, v16, s17
	v_perm_b32 v1, v19, v18, s17
	v_perm_b32 v2, v21, v20, s17
	v_perm_b32 v3, v23, v22, s17
	global_store_dwordx4 v5, v[0:3], s[6:7]
	s_endpgm

.LBB1_12:
	s_and_b32 s12, s19, 1
	s_lshr_b32 s13, s19, 1
	s_add_i32 s16, s19, 1
	v_lshl_add_u32 v231, s13, 3, v221
	s_cmp_lg_u32 s19, 3
	s_cselect_b32 s17, s16, 3
	s_waitcnt lgkmcnt(2)
	v_lshlrev_b32_e32 v2, 7, v231
	s_lshl_b32 s14, s12, 6
	v_or3_b32 v160, v2, s14, v220
	s_waitcnt lgkmcnt(0)
	v_mov_b32_e32 v1, v220
	v_lshl_add_u64 v[2:3], v[160:161], 2, s[6:7]
	global_load_dword v232, v[2:3], off
	s_lshl_b32 s14, s17, 2
	s_and_b32 s14, s14, 24
	s_lshl_b32 s13, s13, 9
	v_lshrrev_b32_e32 v3, 5, v1
	s_cmp_eq_u32 s12, 0
	v_add_u32_e32 v2, s14, v221
	v_lshlrev_b32_e32 v206, 4, v3
	s_cselect_b64 s[14:15], -1, 0
	s_cmp_eq_u32 s12, 1
	v_add3_u32 v149, v228, s13, v206
	s_cselect_b64 s[12:13], -1, 0
	s_lshl_b32 s17, s17, 6
	s_and_b32 s17, s17, 64
	v_lshl_or_b32 v2, v2, 7, s17
	v_lshl_add_u32 v234, v1, 4, 0
	v_and_or_b32 v1, v1, 31, v2
	v_mul_lo_u32 v2, v1, 27
	v_add_u32_e32 v233, 0xc000, v234
	v_mad_u64_u32 v[204:205], s[20:21], v3, 14, v[2:3]
	v_add_u32_e32 v202, 13, v2
	s_waitcnt vmcnt(3)
	v_mul_f32_e32 v1, 0.15915494, v222
	v_cos_f32_e32 v2, v1
	v_sin_f32_e32 v1, v1
	v_add_f32_e32 v2, v2, v2
	v_cndmask_b32_e64 v3, v2, v1, s[0:1]
	v_mul_f32_e32 v1, v1, v2
	v_fma_f32 v2, v2, v2, -2.0
	v_cndmask_b32_e64 v4, v2, v1, s[0:1]
	v_mul_f32_e32 v207, v1, v2
	v_fma_f32 v208, v2, v2, -2.0
	v_mul_f32_e32 v2, 0.15915494, v182
	v_cvt_pk_fp8_f32 v131, v225, v3
	v_cos_f32_e32 v3, v2
	v_sin_f32_e32 v2, v2
	v_cndmask_b32_e64 v1, v208, v207, s[0:1]
	v_cvt_pk_fp8_f32 v131, v4, v1 op_sel:[0,0,1]
	v_add_f32_e32 v1, v3, v3
	v_cvt_pk_f16_f32 v1, v2, v1
	v_cvt_pk_fp8_f32 v128, v182, v0
	v_cvt_scalef32_pk_fp8_f16 v132, v1, 1.0
	v_pk_fma_f16 v1, v1, v1, -2.0 op_sel:[1,0,1] op_sel_hi:[1,1,0]
	v_mul_f32_e32 v0, 0.15915494, v0
	v_cvt_scalef32_pk_fp8_f16 v132, v1, 1.0 op_sel:[0,0,1]
	v_pk_fma_f16 v1, v1, v1, -2.0 op_sel:[0,1,1] op_sel_hi:[1,1,0]
	v_cos_f32_e32 v2, v0
	v_cvt_scalef32_pk_fp8_f16 v133, v1, 1.0
	v_pk_fma_f16 v1, v1, v1, -2.0 op_sel:[0,1,1] op_sel_hi:[1,1,0]
	v_sin_f32_e32 v0, v0
	v_cvt_scalef32_pk_fp8_f16 v133, v1, 1.0 op_sel:[0,0,1]
	v_pk_fma_f16 v1, v1, v1, -2.0 op_sel:[0,1,1] op_sel_hi:[1,1,0]
	s_nop 0
	v_cvt_scalef32_pk_fp8_f16 v134, v1, 1.0
	v_pk_fma_f16 v1, v1, v1, -2.0 op_sel:[0,1,1] op_sel_hi:[1,1,0]
	s_nop 0
	v_cvt_scalef32_pk_fp8_f16 v134, v1, 1.0 op_sel:[0,0,1]
	v_add_f32_e32 v1, v2, v2
	v_cvt_pk_f16_f32 v0, v0, v1
	v_cvt_scalef32_pk_fp8_f16 v135, v0, 1.0
	v_pk_fma_f16 v24, v0, v0, -2.0 op_sel:[1,0,1] op_sel_hi:[1,1,0]
	s_waitcnt vmcnt(2)
	v_mul_f32_e32 v0, 0.15915494, v224
	v_cos_f32_e32 v1, v0
	v_sin_f32_e32 v0, v0
	v_add_f32_e32 v1, v1, v1
	v_cndmask_b32_e64 v2, v1, v0, s[0:1]
	v_mul_f32_e32 v0, v0, v1
	v_fma_f32 v1, v1, v1, -2.0
	v_cndmask_b32_e64 v3, v1, v0, s[0:1]
	v_mul_f32_e32 v209, v0, v1
	v_fma_f32 v210, v1, v1, -2.0
	v_mul_f32_e32 v1, 0.15915494, v190
	s_waitcnt vmcnt(1)
	v_cvt_pk_fp8_f32 v19, v223, v2
	v_cos_f32_e32 v2, v1
	v_sin_f32_e32 v1, v1
	v_cndmask_b32_e64 v0, v210, v209, s[0:1]
	v_cvt_pk_fp8_f32 v19, v3, v0 op_sel:[0,0,1]
	v_add_f32_e32 v0, v2, v2
	v_cvt_pk_f16_f32 v0, v1, v0
	v_cvt_scalef32_pk_fp8_f16 v20, v0, 1.0
	v_pk_fma_f16 v0, v0, v0, -2.0 op_sel:[1,0,1] op_sel_hi:[1,1,0]
	v_mul_f32_e32 v1, 0.15915494, v191
	v_cvt_scalef32_pk_fp8_f16 v135, v24, 1.0 op_sel:[0,0,1]
	v_cvt_scalef32_pk_fp8_f16 v20, v0, 1.0 op_sel:[0,0,1]
	v_pk_fma_f16 v0, v0, v0, -2.0 op_sel:[0,1,1] op_sel_hi:[1,1,0]
	v_cos_f32_e32 v2, v1
	v_pk_fma_f16 v24, v24, v24, -2.0 op_sel:[0,1,1] op_sel_hi:[1,1,0]
	v_cvt_scalef32_pk_fp8_f16 v21, v0, 1.0
	v_pk_fma_f16 v0, v0, v0, -2.0 op_sel:[0,1,1] op_sel_hi:[1,1,0]
	v_sin_f32_e32 v1, v1
	v_pk_fma_f16 v35, v24, v24, -2.0 op_sel:[0,1,1] op_sel_hi:[1,1,0]
	v_cvt_pk_fp8_f32 v128, v25, v185 op_sel:[0,0,1]
	v_cvt_scalef32_pk_fp8_f16 v21, v0, 1.0 op_sel:[0,0,1]
	v_pk_fma_f16 v0, v0, v0, -2.0 op_sel:[0,1,1] op_sel_hi:[1,1,0]
	v_pk_fma_f16 v36, v35, v35, -2.0 op_sel:[0,1,1] op_sel_hi:[1,1,0]
	v_mul_f32_e32 v25, 0.15915494, v25
	v_cvt_pk_fp8_f32 v129, v198, v162
	v_cvt_pk_fp8_f32 v130, v178, v200
	v_cvt_pk_fp8_f32 v16, v190, v191
	v_cvt_pk_fp8_f32 v17, v194, v195
	v_cvt_pk_fp8_f32 v18, v186, v187
	v_cvt_scalef32_pk_fp8_f16 v22, v0, 1.0
	v_pk_fma_f16 v0, v0, v0, -2.0 op_sel:[0,1,1] op_sel_hi:[1,1,0]
	v_pk_fma_f16 v37, v36, v36, -2.0 op_sel:[0,1,1] op_sel_hi:[1,1,0]
	v_cvt_scalef32_pk_fp8_f16 v137, v36, 1.0
	v_cos_f32_e32 v36, v25
	v_cvt_scalef32_pk_fp8_f16 v22, v0, 1.0 op_sel:[0,0,1]
	v_add_f32_e32 v0, v2, v2
	v_sin_f32_e32 v25, v25
	v_cvt_pk_f16_f32 v0, v1, v0
	v_mov_b32_e32 v160, v204
	v_cvt_scalef32_pk_fp8_f16 v23, v0, 1.0
	v_pk_fma_f16 v34, v0, v0, -2.0 op_sel:[1,0,1] op_sel_hi:[1,1,0]
	ds_read_b128 v[26:29], v234
	ds_read_b128 v[30:33], v234 offset:1024
	ds_read_b128 v[8:11], v234 offset:2048
	ds_read_b128 v[12:15], v234 offset:3072
	ds_read_b128 v[0:3], v234 offset:4096
	ds_read_b128 v[4:7], v234 offset:5120
	ds_read_b128 v[152:155], v234 offset:6144
	ds_read_b128 v[156:159], v234 offset:7168
	ds_read_b128 v[96:99], v149
	ds_read_b128 v[100:103], v149 offset:32
	ds_read_b128 v[104:107], v149 offset:64
	ds_read_b128 v[108:111], v149 offset:96
	v_cvt_pk_fp8_f32 v129, v163, v201 op_sel:[0,0,1]
	v_cvt_pk_fp8_f32 v130, v179, v181 op_sel:[0,0,1]
	v_cvt_pk_fp8_f32 v16, v192, v193 op_sel:[0,0,1]
	v_cvt_pk_fp8_f32 v17, v196, v197 op_sel:[0,0,1]
	v_cvt_pk_fp8_f32 v18, v188, v189 op_sel:[0,0,1]
	v_cvt_scalef32_pk_fp8_f16 v136, v24, 1.0
	v_add_f32_e32 v24, v36, v36
	v_cvt_pk_f16_f32 v24, v25, v24
	v_pk_fma_f16 v25, v24, v24, -2.0 op_sel:[1,0,1] op_sel_hi:[1,1,0]
	v_cvt_scalef32_pk_fp8_f16 v138, v24, 1.0
	v_cvt_scalef32_pk_fp8_f16 v23, v34, 1.0 op_sel:[0,0,1]
	v_cvt_scalef32_pk_fp8_f16 v136, v35, 1.0 op_sel:[0,0,1]
	v_pk_fma_f16 v35, v25, v25, -2.0 op_sel:[0,1,1] op_sel_hi:[1,1,0]
	v_cvt_scalef32_pk_fp8_f16 v138, v25, 1.0 op_sel:[0,0,1]
	v_mul_f32_e32 v25, 0.15915494, v185
	s_waitcnt lgkmcnt(0)
	v_mfma_scale_f32_32x32x64_f8f6f4 v[112:127], v[26:33], v[16:23], v[96:111], v227, v226 op_sel_hi:[0,0,0]
	v_cvt_scalef32_pk_fp8_f16 v139, v35, 1.0
	v_pk_fma_f16 v35, v35, v35, -2.0 op_sel:[0,1,1] op_sel_hi:[1,1,0]
	s_nop 0
	v_pk_fma_f16 v24, v35, v35, -2.0 op_sel:[0,1,1] op_sel_hi:[1,1,0]
	ds_read_b128 v[64:67], v149 offset:128
	ds_read_b128 v[68:71], v149 offset:160
	ds_read_b128 v[72:75], v149 offset:192
	ds_read_b128 v[76:79], v149 offset:224
	v_cvt_scalef32_pk_fp8_f16 v140, v24, 1.0
	v_pk_fma_f16 v24, v24, v24, -2.0 op_sel:[0,1,1] op_sel_hi:[1,1,0]
	v_cvt_scalef32_pk_fp8_f16 v137, v37, 1.0 op_sel:[0,0,1]
	v_cvt_scalef32_pk_fp8_f16 v140, v24, 1.0 op_sel:[0,0,1]
	v_cvt_scalef32_pk_fp8_f16 v139, v35, 1.0 op_sel:[0,0,1]
	v_mfma_scale_f32_32x32x64_f8f6f4 v[96:111], v[26:33], v[128:135], v[96:111], v227, v226 op_sel_hi:[0,0,0]
	v_cos_f32_e32 v26, v25
	v_sin_f32_e32 v25, v25
	v_mul_f32_e32 v30, 0.15915494, v192
	v_mul_f32_e32 v31, 0.15915494, v193
	v_add_f32_e32 v24, v26, v26
	v_cvt_pk_f16_f32 v24, v25, v24
	v_cvt_scalef32_pk_fp8_f16 v141, v24, 1.0
	v_pk_fma_f16 v24, v24, v24, -2.0 op_sel:[1,0,1] op_sel_hi:[1,1,0]
	s_nop 0
	v_cvt_scalef32_pk_fp8_f16 v141, v24, 1.0 op_sel:[0,0,1]
	v_pk_fma_f16 v26, v24, v24, -2.0 op_sel:[0,1,1] op_sel_hi:[1,1,0]
	v_lshl_add_u64 v[24:25], v[160:161], 2, s[4:5]
	v_pk_fma_f16 v27, v26, v26, -2.0 op_sel:[0,1,1] op_sel_hi:[1,1,0]
	s_nop 0
	v_pk_fma_f16 v28, v27, v27, -2.0 op_sel:[0,1,1] op_sel_hi:[1,1,0]
	s_waitcnt lgkmcnt(0)
	v_mfma_scale_f32_32x32x64_f8f6f4 v[80:95], v[8:15], v[16:23], v[64:79], v227, v226 op_sel_hi:[0,0,0]
	global_load_dwordx4 v[182:185], v[24:25], off
	global_load_dwordx4 v[190:193], v[24:25], off offset:3456
	v_cos_f32_e32 v25, v31
	v_pk_fma_f16 v29, v28, v28, -2.0 op_sel:[0,1,1] op_sel_hi:[1,1,0]
	v_cvt_scalef32_pk_fp8_f16 v143, v28, 1.0
	v_cvt_scalef32_pk_fp8_f16 v142, v26, 1.0
	v_cvt_scalef32_pk_fp8_f16 v143, v29, 1.0 op_sel:[0,0,1]
	v_cvt_scalef32_pk_fp8_f16 v142, v27, 1.0 op_sel:[0,0,1]
	v_add_f32_e32 v150, v25, v25
	v_mfma_scale_f32_32x32x64_f8f6f4 v[64:79], v[8:15], v[128:135], v[64:79], v227, v226 op_sel_hi:[0,0,0]
	v_pk_fma_f16 v8, v34, v34, -2.0 op_sel:[0,1,1] op_sel_hi:[1,1,0]
	ds_read_b128 v[32:35], v149 offset:256
	ds_read_b128 v[36:39], v149 offset:288
	ds_read_b128 v[40:43], v149 offset:320
	ds_read_b128 v[44:47], v149 offset:352
	v_pk_fma_f16 v9, v8, v8, -2.0 op_sel:[0,1,1] op_sel_hi:[1,1,0]
	v_cvt_scalef32_pk_fp8_f16 v144, v8, 1.0
	v_pk_fma_f16 v10, v9, v9, -2.0 op_sel:[0,1,1] op_sel_hi:[1,1,0]
	v_cvt_scalef32_pk_fp8_f16 v144, v9, 1.0 op_sel:[0,0,1]
	v_pk_fma_f16 v11, v10, v10, -2.0 op_sel:[0,1,1] op_sel_hi:[1,1,0]
	v_cvt_scalef32_pk_fp8_f16 v145, v10, 1.0
	v_cos_f32_e32 v10, v30
	v_cvt_scalef32_pk_fp8_f16 v145, v11, 1.0 op_sel:[0,0,1]
	v_sin_f32_e32 v11, v30
	v_add_f32_e32 v8, v10, v10
	v_cvt_pk_f16_f32 v8, v11, v8
	v_pk_fma_f16 v9, v8, v8, -2.0 op_sel:[1,0,1] op_sel_hi:[1,1,0]
	v_cvt_scalef32_pk_fp8_f16 v146, v8, 1.0
	v_pk_fma_f16 v10, v9, v9, -2.0 op_sel:[0,1,1] op_sel_hi:[1,1,0]
	s_waitcnt lgkmcnt(0)
	v_mfma_scale_f32_32x32x64_f8f6f4 v[48:63], v[0:7], v[16:23], v[32:47], v227, v226 op_sel_hi:[0,0,0]
	v_cvt_scalef32_pk_fp8_f16 v147, v10, 1.0
	v_pk_fma_f16 v10, v10, v10, -2.0 op_sel:[0,1,1] op_sel_hi:[1,1,0]
	v_cvt_scalef32_pk_fp8_f16 v146, v9, 1.0 op_sel:[0,0,1]
	v_cvt_scalef32_pk_fp8_f16 v147, v10, 1.0 op_sel:[0,0,1]
	v_pk_fma_f16 v24, v10, v10, -2.0 op_sel:[0,1,1] op_sel_hi:[1,1,0]
	s_nop 0
	v_cvt_scalef32_pk_fp8_f16 v148, v24, 1.0
	v_pk_fma_f16 v24, v24, v24, -2.0 op_sel:[0,1,1] op_sel_hi:[1,1,0]
	s_nop 0
	v_cvt_scalef32_pk_fp8_f16 v148, v24, 1.0 op_sel:[0,0,1]
	v_mfma_scale_f32_32x32x64_f8f6f4 v[32:47], v[0:7], v[128:135], v[32:47], v227, v226 op_sel_hi:[0,0,0]
	ds_read_b128 v[0:3], v149 offset:384
	ds_read_b128 v[4:7], v149 offset:416
	ds_read_b128 v[8:11], v149 offset:448
	ds_read_b128 v[12:15], v149 offset:480
	v_sin_f32_e32 v149, v31
	s_nop 0
	v_cvt_pk_f16_f32 v150, v149, v150
	v_cvt_scalef32_pk_fp8_f16 v149, v150, 1.0
	v_pk_fma_f16 v150, v150, v150, -2.0 op_sel:[1,0,1] op_sel_hi:[1,1,0]
	s_nop 0
	v_pk_fma_f16 v160, v150, v150, -2.0 op_sel:[0,1,1] op_sel_hi:[1,1,0]
	v_cvt_scalef32_pk_fp8_f16 v149, v150, 1.0 op_sel:[0,0,1]
	v_pk_fma_f16 v164, v160, v160, -2.0 op_sel:[0,1,1] op_sel_hi:[1,1,0]
	s_nop 0
	v_pk_fma_f16 v150, v164, v164, -2.0 op_sel:[0,1,1] op_sel_hi:[1,1,0]
	s_waitcnt lgkmcnt(0)
	v_mfma_scale_f32_32x32x64_f8f6f4 v[16:31], v[152:159], v[16:23], v[0:15], v227, v226 op_sel_hi:[0,0,0]
	v_pk_fma_f16 v165, v150, v150, -2.0 op_sel:[0,1,1] op_sel_hi:[1,1,0]
	v_cvt_scalef32_pk_fp8_f16 v151, v150, 1.0
	v_cvt_scalef32_pk_fp8_f16 v150, v160, 1.0
	v_cvt_scalef32_pk_fp8_f16 v151, v165, 1.0 op_sel:[0,0,1]
	v_cvt_scalef32_pk_fp8_f16 v150, v164, 1.0 op_sel:[0,0,1]
	v_mfma_scale_f32_32x32x64_f8f6f4 v[0:15], v[152:159], v[128:135], v[0:15], v227, v226 op_sel_hi:[0,0,0]
	v_mul_f32_e32 v128, 0.15915494, v198
	v_cos_f32_e32 v129, v128
	v_sin_f32_e32 v128, v128
	v_mul_f32_e32 v133, 0.15915494, v162
	v_cos_f32_e32 v134, v133
	v_add_f32_e32 v129, v129, v129
	v_cvt_pk_f16_f32 v130, v128, v129
	v_pk_fma_f16 v131, v130, v130, -2.0 op_sel:[1,0,1] op_sel_hi:[1,1,0]
	v_sin_f32_e32 v133, v133
	v_pk_fma_f16 v128, v131, v131, -2.0 op_sel:[0,1,1] op_sel_hi:[1,1,0]
	s_nop 0
	v_pk_fma_f16 v132, v128, v128, -2.0 op_sel:[0,1,1] op_sel_hi:[1,1,0]
	v_cvt_scalef32_pk_fp8_f16 v129, v128, 1.0
	v_cvt_scalef32_pk_fp8_f16 v128, v130, 1.0
	v_add_f32_e32 v130, v134, v134
	v_cvt_scalef32_pk_fp8_f16 v128, v131, 1.0 op_sel:[0,0,1]
	v_cvt_pk_f16_f32 v130, v133, v130
	v_cvt_scalef32_pk_fp8_f16 v129, v132, 1.0 op_sel:[0,0,1]
	v_cvt_scalef32_pk_fp8_f16 v131, v130, 1.0
	v_pk_fma_f16 v133, v130, v130, -2.0 op_sel:[1,0,1] op_sel_hi:[1,1,0]
	v_pk_fma_f16 v132, v132, v132, -2.0 op_sel:[0,1,1] op_sel_hi:[1,1,0]
	ds_read_b128 v[152:155], v234 offset:8192
	ds_read_b128 v[156:159], v234 offset:9216
	ds_read_b128 v[164:167], v234 offset:10240
	ds_read_b128 v[168:171], v234 offset:11264
	ds_read_b128 v[236:239], v234 offset:12288
	ds_read_b128 v[240:243], v234 offset:13312
	v_cvt_scalef32_pk_fp8_f16 v130, v132, 1.0
	v_pk_fma_f16 v132, v132, v132, -2.0 op_sel:[0,1,1] op_sel_hi:[1,1,0]
	v_mul_f32_e32 v135, 0.15915494, v163
	s_waitcnt lgkmcnt(4)
	v_mfma_scale_f32_32x32x64_f8f6f4 v[96:111], v[152:159], v[136:143], v[96:111], v227, v226 op_sel_hi:[0,0,0]
	v_cvt_scalef32_pk_fp8_f16 v131, v133, 1.0 op_sel:[0,0,1]
	v_pk_fma_f16 v133, v133, v133, -2.0 op_sel:[0,1,1] op_sel_hi:[1,1,0]
	v_cvt_scalef32_pk_fp8_f16 v130, v132, 1.0 op_sel:[0,0,1]
	v_cvt_scalef32_pk_fp8_f16 v132, v133, 1.0
	v_pk_fma_f16 v133, v133, v133, -2.0 op_sel:[0,1,1] op_sel_hi:[1,1,0]
	ds_read_b128 v[244:247], v234 offset:14336
	ds_read_b128 v[248:251], v234 offset:15360
	v_pk_fma_f16 v134, v133, v133, -2.0 op_sel:[0,1,1] op_sel_hi:[1,1,0]
	v_cvt_scalef32_pk_fp8_f16 v132, v133, 1.0 op_sel:[0,0,1]
	v_cvt_scalef32_pk_fp8_f16 v133, v134, 1.0
	v_pk_fma_f16 v134, v134, v134, -2.0 op_sel:[0,1,1] op_sel_hi:[1,1,0]
	s_nop 0
	v_cvt_scalef32_pk_fp8_f16 v133, v134, 1.0 op_sel:[0,0,1]
	v_mfma_scale_f32_32x32x64_f8f6f4 v[112:127], v[152:159], v[144:151], v[112:127], v227, v226 op_sel_hi:[0,0,0]
	v_cos_f32_e32 v152, v135
	v_sin_f32_e32 v135, v135
	v_mul_f32_e32 v154, 0.15915494, v194
	v_cos_f32_e32 v155, v154
	v_add_f32_e32 v134, v152, v152
	v_cvt_pk_f16_f32 v152, v135, v134
	v_pk_fma_f16 v153, v152, v152, -2.0 op_sel:[1,0,1] op_sel_hi:[1,1,0]
	v_sin_f32_e32 v154, v154
	v_pk_fma_f16 v134, v153, v153, -2.0 op_sel:[0,1,1] op_sel_hi:[1,1,0]
	s_nop 0
	v_pk_fma_f16 v160, v134, v134, -2.0 op_sel:[0,1,1] op_sel_hi:[1,1,0]
	v_cvt_scalef32_pk_fp8_f16 v135, v134, 1.0
	v_cvt_scalef32_pk_fp8_f16 v134, v152, 1.0
	v_add_f32_e32 v152, v155, v155
	s_waitcnt lgkmcnt(4)
	v_mfma_scale_f32_32x32x64_f8f6f4 v[64:79], v[164:171], v[136:143], v[64:79], v227, v226 op_sel_hi:[0,0,0]
	v_mul_f32_e32 v157, 0.15915494, v195
	v_cvt_pk_f16_f32 v154, v154, v152
	v_cos_f32_e32 v158, v157
	v_pk_fma_f16 v155, v154, v154, -2.0 op_sel:[1,0,1] op_sel_hi:[1,1,0]
	v_sin_f32_e32 v157, v157
	v_pk_fma_f16 v152, v155, v155, -2.0 op_sel:[0,1,1] op_sel_hi:[1,1,0]
	v_cvt_scalef32_pk_fp8_f16 v134, v153, 1.0 op_sel:[0,0,1]
	v_pk_fma_f16 v156, v152, v152, -2.0 op_sel:[0,1,1] op_sel_hi:[1,1,0]
	v_cvt_scalef32_pk_fp8_f16 v153, v152, 1.0
	v_cvt_scalef32_pk_fp8_f16 v152, v154, 1.0
	v_add_f32_e32 v154, v158, v158
	v_mul_f32_e32 v159, 0.15915494, v196
	v_cvt_scalef32_pk_fp8_f16 v152, v155, 1.0 op_sel:[0,0,1]
	v_mfma_scale_f32_32x32x64_f8f6f4 v[80:95], v[164:171], v[144:151], v[80:95], v227, v226 op_sel_hi:[0,0,0]
	v_cvt_pk_f16_f32 v154, v157, v154
	v_cvt_scalef32_pk_fp8_f16 v153, v156, 1.0 op_sel:[0,0,1]
	v_cvt_scalef32_pk_fp8_f16 v155, v154, 1.0
	v_pk_fma_f16 v156, v156, v156, -2.0 op_sel:[0,1,1] op_sel_hi:[1,1,0]
	v_pk_fma_f16 v157, v154, v154, -2.0 op_sel:[1,0,1] op_sel_hi:[1,1,0]
	v_cvt_scalef32_pk_fp8_f16 v154, v156, 1.0
	v_pk_fma_f16 v156, v156, v156, -2.0 op_sel:[0,1,1] op_sel_hi:[1,1,0]
	v_cvt_scalef32_pk_fp8_f16 v155, v157, 1.0 op_sel:[0,0,1]
	v_pk_fma_f16 v157, v157, v157, -2.0 op_sel:[0,1,1] op_sel_hi:[1,1,0]
	v_cvt_scalef32_pk_fp8_f16 v154, v156, 1.0 op_sel:[0,0,1]
	v_cvt_scalef32_pk_fp8_f16 v156, v157, 1.0
	v_pk_fma_f16 v157, v157, v157, -2.0 op_sel:[0,1,1] op_sel_hi:[1,1,0]
	s_waitcnt lgkmcnt(0)
	v_mfma_scale_f32_32x32x64_f8f6f4 v[0:15], v[244:251], v[136:143], v[0:15], v227, v226 op_sel_hi:[0,0,0]
	v_cvt_scalef32_pk_fp8_f16 v156, v157, 1.0 op_sel:[0,0,1]
	v_pk_fma_f16 v158, v157, v157, -2.0 op_sel:[0,1,1] op_sel_hi:[1,1,0]
	v_cvt_scalef32_pk_fp8_f16 v135, v160, 1.0 op_sel:[0,0,1]
	v_cvt_scalef32_pk_fp8_f16 v157, v158, 1.0
	v_mfma_scale_f32_32x32x64_f8f6f4 v[32:47], v[236:243], v[136:143], v[32:47], v227, v226 op_sel_hi:[0,0,0]
	v_cos_f32_e32 v136, v159
	v_sin_f32_e32 v137, v159
	v_pk_fma_f16 v138, v158, v158, -2.0 op_sel:[0,1,1] op_sel_hi:[1,1,0]
	v_add_f32_e32 v136, v136, v136
	v_cvt_pk_f16_f32 v136, v137, v136
	v_pk_fma_f16 v137, v136, v136, -2.0 op_sel:[1,0,1] op_sel_hi:[1,1,0]
	v_cvt_scalef32_pk_fp8_f16 v157, v138, 1.0 op_sel:[0,0,1]
	v_pk_fma_f16 v138, v137, v137, -2.0 op_sel:[0,1,1] op_sel_hi:[1,1,0]
	s_nop 0
	v_pk_fma_f16 v180, v138, v138, -2.0 op_sel:[0,1,1] op_sel_hi:[1,1,0]
	v_cvt_scalef32_pk_fp8_f16 v159, v138, 1.0
	v_cvt_scalef32_pk_fp8_f16 v158, v136, 1.0
	v_cvt_scalef32_pk_fp8_f16 v159, v180, 1.0 op_sel:[0,0,1]
	v_cvt_scalef32_pk_fp8_f16 v158, v137, 1.0 op_sel:[0,0,1]
	v_mfma_scale_f32_32x32x64_f8f6f4 v[48:63], v[236:243], v[144:151], v[48:63], v227, v226 op_sel_hi:[0,0,0]
	v_mfma_scale_f32_32x32x64_f8f6f4 v[16:31], v[244:251], v[144:151], v[16:31], v227, v226 op_sel_hi:[0,0,0]
	ds_read_b128 v[140:143], v234 offset:16384
	ds_read_b128 v[144:147], v234 offset:17408
	ds_read_b128 v[236:239], v234 offset:18432
	ds_read_b128 v[240:243], v234 offset:19456
	ds_read_b128 v[170:173], v234 offset:20480
	ds_read_b128 v[174:177], v234 offset:21504
	s_waitcnt lgkmcnt(4)
	v_mfma_scale_f32_32x32x64_f8f6f4 v[96:111], v[140:147], v[128:135], v[96:111], v227, v226 op_sel_hi:[0,0,0]
	v_pk_fma_f16 v139, v160, v160, -2.0 op_sel:[0,1,1] op_sel_hi:[1,1,0]
	v_mov_b32_e32 v160, v204
	ds_read_b128 v[162:165], v234 offset:22528
	ds_read_b128 v[166:169], v234 offset:23552
	v_mul_f32_e32 v136, 0.15915494, v201
	v_cos_f32_e32 v137, v136
	v_sin_f32_e32 v136, v136
	v_mul_f32_e32 v150, 0.15915494, v186
	v_cos_f32_e32 v151, v150
	v_add_f32_e32 v137, v137, v137
	v_cvt_pk_f16_f32 v136, v136, v137
	v_pk_fma_f16 v138, v136, v136, -2.0 op_sel:[1,0,1] op_sel_hi:[1,1,0]
	v_cvt_scalef32_pk_fp8_f16 v137, v136, 1.0
	v_mfma_scale_f32_32x32x64_f8f6f4 v[112:127], v[140:147], v[152:159], v[112:127], v227, v226 op_sel_hi:[0,0,0]
	v_mul_f32_e32 v140, 0.15915494, v178
	v_cos_f32_e32 v141, v140
	v_sin_f32_e32 v140, v140
	v_mul_f32_e32 v143, 0.15915494, v200
	v_cos_f32_e32 v144, v143
	v_add_f32_e32 v141, v141, v141
	v_cvt_pk_f16_f32 v141, v140, v141
	v_sin_f32_e32 v143, v143
	v_cvt_scalef32_pk_fp8_f16 v140, v141, 1.0
	v_pk_fma_f16 v141, v141, v141, -2.0 op_sel:[1,0,1] op_sel_hi:[1,1,0]
	v_mul_f32_e32 v146, 0.15915494, v197
	v_pk_fma_f16 v142, v141, v141, -2.0 op_sel:[0,1,1] op_sel_hi:[1,1,0]
	v_cvt_scalef32_pk_fp8_f16 v140, v141, 1.0 op_sel:[0,0,1]
	v_cvt_scalef32_pk_fp8_f16 v141, v142, 1.0
	v_pk_fma_f16 v145, v142, v142, -2.0 op_sel:[0,1,1] op_sel_hi:[1,1,0]
	v_add_f32_e32 v142, v144, v144
	v_cvt_pk_f16_f32 v144, v143, v142
	v_lshl_add_u64 v[142:143], v[160:161], 2, s[4:5]
	global_load_dwordx4 v[198:201], v[142:143], off offset:16
	global_load_dwordx4 v[194:197], v[142:143], off offset:3472
	v_cvt_scalef32_pk_fp8_f16 v141, v145, 1.0 op_sel:[0,0,1]
	v_pk_fma_f16 v160, v144, v144, -2.0 op_sel:[1,0,1] op_sel_hi:[1,1,0]
	v_cvt_scalef32_pk_fp8_f16 v143, v144, 1.0
	v_pk_fma_f16 v144, v145, v145, -2.0 op_sel:[0,1,1] op_sel_hi:[1,1,0]
	v_cos_f32_e32 v145, v146
	v_sin_f32_e32 v146, v146
	v_pk_fma_f16 v148, v138, v138, -2.0 op_sel:[0,1,1] op_sel_hi:[1,1,0]
	v_cvt_scalef32_pk_fp8_f16 v136, v139, 1.0
	v_pk_fma_f16 v139, v139, v139, -2.0 op_sel:[0,1,1] op_sel_hi:[1,1,0]
	v_pk_fma_f16 v149, v148, v148, -2.0 op_sel:[0,1,1] op_sel_hi:[1,1,0]
	v_cvt_scalef32_pk_fp8_f16 v142, v144, 1.0
	v_pk_fma_f16 v144, v144, v144, -2.0 op_sel:[0,1,1] op_sel_hi:[1,1,0]
	v_cvt_scalef32_pk_fp8_f16 v137, v138, 1.0 op_sel:[0,0,1]
	v_cvt_scalef32_pk_fp8_f16 v136, v139, 1.0 op_sel:[0,0,1]
	v_pk_fma_f16 v138, v149, v149, -2.0 op_sel:[0,1,1] op_sel_hi:[1,1,0]
	v_cvt_scalef32_pk_fp8_f16 v142, v144, 1.0 op_sel:[0,0,1]
	v_add_f32_e32 v144, v145, v145
	v_cvt_scalef32_pk_fp8_f16 v139, v138, 1.0
	v_pk_fma_f16 v138, v138, v138, -2.0 op_sel:[0,1,1] op_sel_hi:[1,1,0]
	s_waitcnt lgkmcnt(4)
	v_mfma_scale_f32_32x32x64_f8f6f4 v[64:79], v[236:243], v[128:135], v[64:79], v227, v226 op_sel_hi:[0,0,0]
	v_cvt_pk_f16_f32 v144, v146, v144
	v_cvt_scalef32_pk_fp8_f16 v139, v138, 1.0 op_sel:[0,0,1]
	v_pk_fma_f16 v146, v144, v144, -2.0 op_sel:[1,0,1] op_sel_hi:[1,1,0]
	v_cvt_scalef32_pk_fp8_f16 v138, v148, 1.0
	v_cvt_scalef32_pk_fp8_f16 v145, v144, 1.0
	v_pk_fma_f16 v147, v180, v180, -2.0 op_sel:[0,1,1] op_sel_hi:[1,1,0]
	v_pk_fma_f16 v148, v146, v146, -2.0 op_sel:[0,1,1] op_sel_hi:[1,1,0]
	v_cvt_scalef32_pk_fp8_f16 v138, v149, 1.0 op_sel:[0,0,1]
	v_cvt_scalef32_pk_fp8_f16 v144, v147, 1.0
	v_pk_fma_f16 v147, v147, v147, -2.0 op_sel:[0,1,1] op_sel_hi:[1,1,0]
	v_pk_fma_f16 v149, v148, v148, -2.0 op_sel:[0,1,1] op_sel_hi:[1,1,0]
	v_cvt_scalef32_pk_fp8_f16 v145, v146, 1.0 op_sel:[0,0,1]
	v_mfma_scale_f32_32x32x64_f8f6f4 v[80:95], v[236:243], v[152:159], v[80:95], v227, v226 op_sel_hi:[0,0,0]
	v_pk_fma_f16 v146, v149, v149, -2.0 op_sel:[0,1,1] op_sel_hi:[1,1,0]
	v_cvt_scalef32_pk_fp8_f16 v144, v147, 1.0 op_sel:[0,0,1]
	v_cvt_scalef32_pk_fp8_f16 v147, v146, 1.0
	v_pk_fma_f16 v146, v146, v146, -2.0 op_sel:[0,1,1] op_sel_hi:[1,1,0]
	v_sin_f32_e32 v150, v150
	v_cvt_scalef32_pk_fp8_f16 v147, v146, 1.0 op_sel:[0,0,1]
	v_cvt_scalef32_pk_fp8_f16 v146, v148, 1.0
	v_add_f32_e32 v148, v151, v151
	v_mul_f32_e32 v151, 0.15915494, v187
	v_cvt_scalef32_pk_fp8_f16 v146, v149, 1.0 op_sel:[0,0,1]
	v_cvt_pk_f16_f32 v149, v150, v148
	v_cvt_scalef32_pk_fp8_f16 v148, v149, 1.0
	s_waitcnt lgkmcnt(0)
	v_mfma_scale_f32_32x32x64_f8f6f4 v[0:15], v[162:169], v[128:135], v[0:15], v227, v226 op_sel_hi:[0,0,0]
	v_pk_fma_f16 v149, v149, v149, -2.0 op_sel:[1,0,1] op_sel_hi:[1,1,0]
	v_cvt_scalef32_pk_fp8_f16 v143, v160, 1.0 op_sel:[0,0,1]
	v_pk_fma_f16 v150, v149, v149, -2.0 op_sel:[0,1,1] op_sel_hi:[1,1,0]
	v_cvt_scalef32_pk_fp8_f16 v148, v149, 1.0 op_sel:[0,0,1]
	v_cvt_scalef32_pk_fp8_f16 v149, v150, 1.0
	v_mfma_scale_f32_32x32x64_f8f6f4 v[32:47], v[170:177], v[128:135], v[32:47], v227, v226 op_sel_hi:[0,0,0]
	v_cos_f32_e32 v128, v151
	v_sin_f32_e32 v129, v151
	v_pk_fma_f16 v130, v150, v150, -2.0 op_sel:[0,1,1] op_sel_hi:[1,1,0]
	v_add_f32_e32 v128, v128, v128
	v_cvt_pk_f16_f32 v128, v129, v128
	v_pk_fma_f16 v203, v128, v128, -2.0 op_sel:[1,0,1] op_sel_hi:[1,1,0]
	v_cvt_scalef32_pk_fp8_f16 v151, v128, 1.0
	v_pk_fma_f16 v128, v130, v130, -2.0 op_sel:[0,1,1] op_sel_hi:[1,1,0]
	s_nop 0
	v_cvt_scalef32_pk_fp8_f16 v150, v128, 1.0
	v_pk_fma_f16 v128, v128, v128, -2.0 op_sel:[0,1,1] op_sel_hi:[1,1,0]
	v_cvt_scalef32_pk_fp8_f16 v149, v130, 1.0 op_sel:[0,0,1]
	v_cvt_scalef32_pk_fp8_f16 v151, v203, 1.0 op_sel:[0,0,1]
	v_cvt_scalef32_pk_fp8_f16 v150, v128, 1.0 op_sel:[0,0,1]
	v_mfma_scale_f32_32x32x64_f8f6f4 v[48:63], v[170:177], v[152:159], v[48:63], v227, v226 op_sel_hi:[0,0,0]
	v_mfma_scale_f32_32x32x64_f8f6f4 v[16:31], v[162:169], v[152:159], v[16:31], v227, v226 op_sel_hi:[0,0,0]
	v_pk_fma_f16 v130, v160, v160, -2.0 op_sel:[0,1,1] op_sel_hi:[1,1,0]
	s_nop 0
	v_pk_fma_f16 v131, v130, v130, -2.0 op_sel:[0,1,1] op_sel_hi:[1,1,0]
	ds_read_b128 v[152:155], v234 offset:24576
	ds_read_b128 v[156:159], v234 offset:25600
	ds_read_b128 v[162:165], v234 offset:26624
	ds_read_b128 v[166:169], v234 offset:27648
	v_pk_fma_f16 v128, v131, v131, -2.0 op_sel:[0,1,1] op_sel_hi:[1,1,0]
	v_mov_b32_e32 v160, v204
	v_pk_fma_f16 v132, v128, v128, -2.0 op_sel:[0,1,1] op_sel_hi:[1,1,0]
	v_cvt_scalef32_pk_fp8_f16 v129, v128, 1.0
	v_cvt_scalef32_pk_fp8_f16 v129, v132, 1.0 op_sel:[0,0,1]
	v_mul_f32_e32 v132, 0.15915494, v179
	v_sin_f32_e32 v133, v132
	v_cos_f32_e32 v132, v132
	v_cvt_scalef32_pk_fp8_f16 v128, v130, 1.0
	v_cvt_scalef32_pk_fp8_f16 v128, v131, 1.0 op_sel:[0,0,1]
	v_add_f32_e32 v130, v132, v132
	v_cvt_pk_f16_f32 v132, v133, v130
	v_pk_fma_f16 v133, v132, v132, -2.0 op_sel:[1,0,1] op_sel_hi:[1,1,0]
	s_nop 0
	v_pk_fma_f16 v130, v133, v133, -2.0 op_sel:[0,1,1] op_sel_hi:[1,1,0]
	s_waitcnt lgkmcnt(2)
	v_mfma_scale_f32_32x32x64_f8f6f4 v[96:111], v[152:159], v[136:143], v[96:111], v227, v226 op_sel_hi:[0,0,0]
	v_cvt_scalef32_pk_fp8_f16 v131, v130, 1.0
	v_pk_fma_f16 v134, v130, v130, -2.0 op_sel:[0,1,1] op_sel_hi:[1,1,0]
	v_cvt_scalef32_pk_fp8_f16 v130, v132, 1.0
	v_cvt_scalef32_pk_fp8_f16 v131, v134, 1.0 op_sel:[0,0,1]
	v_cvt_scalef32_pk_fp8_f16 v130, v133, 1.0 op_sel:[0,0,1]
	v_pk_fma_f16 v133, v134, v134, -2.0 op_sel:[0,1,1] op_sel_hi:[1,1,0]
	v_mul_f32_e32 v134, 0.15915494, v181
	v_cos_f32_e32 v135, v134
	v_sin_f32_e32 v134, v134
	v_cvt_scalef32_pk_fp8_f16 v132, v133, 1.0
	v_pk_fma_f16 v133, v133, v133, -2.0 op_sel:[0,1,1] op_sel_hi:[1,1,0]
	ds_read_b128 v[170:173], v234 offset:28672
	ds_read_b128 v[174:177], v234 offset:29696
	ds_read_b128 v[236:239], v234 offset:30720
	ds_read_b128 v[240:243], v234 offset:31744
	v_cvt_scalef32_pk_fp8_f16 v132, v133, 1.0 op_sel:[0,0,1]
	v_add_f32_e32 v133, v135, v135
	v_mfma_scale_f32_32x32x64_f8f6f4 v[112:127], v[152:159], v[144:151], v[112:127], v227, v226 op_sel_hi:[0,0,0]
	v_cvt_pk_f16_f32 v152, v134, v133
	v_mul_f32_e32 v153, 0.15915494, v188
	v_lshl_add_u64 v[134:135], v[160:161], 2, s[4:5]
	v_mul_f32_e32 v154, 0.15915494, v189
	global_load_dwordx4 v[178:181], v[134:135], off offset:32
	global_load_dwordx4 v[186:189], v[134:135], off offset:3488
	v_pk_fma_f16 v134, v152, v152, -2.0 op_sel:[1,0,1] op_sel_hi:[1,1,0]
	v_cvt_scalef32_pk_fp8_f16 v133, v152, 1.0
	v_pk_fma_f16 v152, v134, v134, -2.0 op_sel:[0,1,1] op_sel_hi:[1,1,0]
	v_cvt_scalef32_pk_fp8_f16 v133, v134, 1.0 op_sel:[0,0,1]
	v_pk_fma_f16 v155, v152, v152, -2.0 op_sel:[0,1,1] op_sel_hi:[1,1,0]
	s_nop 0
	v_pk_fma_f16 v134, v155, v155, -2.0 op_sel:[0,1,1] op_sel_hi:[1,1,0]
	s_nop 0
	v_pk_fma_f16 v156, v134, v134, -2.0 op_sel:[0,1,1] op_sel_hi:[1,1,0]
	v_cvt_scalef32_pk_fp8_f16 v135, v134, 1.0
	v_cvt_scalef32_pk_fp8_f16 v134, v152, 1.0
	v_pk_fma_f16 v152, v203, v203, -2.0 op_sel:[0,1,1] op_sel_hi:[1,1,0]
	v_cvt_scalef32_pk_fp8_f16 v134, v155, 1.0 op_sel:[0,0,1]
	v_pk_fma_f16 v155, v152, v152, -2.0 op_sel:[0,1,1] op_sel_hi:[1,1,0]
	s_waitcnt lgkmcnt(4)
	v_mfma_scale_f32_32x32x64_f8f6f4 v[64:79], v[162:169], v[136:143], v[64:79], v227, v226 op_sel_hi:[0,0,0]
	v_cvt_scalef32_pk_fp8_f16 v135, v156, 1.0 op_sel:[0,0,1]
	v_pk_fma_f16 v156, v155, v155, -2.0 op_sel:[0,1,1] op_sel_hi:[1,1,0]
	s_nop 0
	v_pk_fma_f16 v157, v156, v156, -2.0 op_sel:[0,1,1] op_sel_hi:[1,1,0]
	v_mfma_scale_f32_32x32x64_f8f6f4 v[80:95], v[162:169], v[144:151], v[80:95], v227, v226 op_sel_hi:[0,0,0]
	v_cvt_scalef32_pk_fp8_f16 v165, v156, 1.0
	v_cos_f32_e32 v156, v153
	v_sin_f32_e32 v153, v153
	v_cvt_scalef32_pk_fp8_f16 v164, v152, 1.0
	v_add_f32_e32 v152, v156, v156
	v_cvt_pk_f16_f32 v152, v153, v152
	v_pk_fma_f16 v153, v152, v152, -2.0 op_sel:[1,0,1] op_sel_hi:[1,1,0]
	v_cvt_scalef32_pk_fp8_f16 v166, v152, 1.0
	v_cvt_scalef32_pk_fp8_f16 v164, v155, 1.0 op_sel:[0,0,1]
	v_pk_fma_f16 v155, v153, v153, -2.0 op_sel:[0,1,1] op_sel_hi:[1,1,0]
	v_cvt_scalef32_pk_fp8_f16 v166, v153, 1.0 op_sel:[0,0,1]
	s_waitcnt lgkmcnt(0)
	v_mfma_scale_f32_32x32x64_f8f6f4 v[0:15], v[236:243], v[136:143], v[0:15], v227, v226 op_sel_hi:[0,0,0]
	v_cos_f32_e32 v153, v154
	v_cvt_scalef32_pk_fp8_f16 v167, v155, 1.0
	v_pk_fma_f16 v155, v155, v155, -2.0 op_sel:[0,1,1] op_sel_hi:[1,1,0]
	v_sin_f32_e32 v154, v154
	v_pk_fma_f16 v152, v155, v155, -2.0 op_sel:[0,1,1] op_sel_hi:[1,1,0]
	s_nop 0
	v_cvt_scalef32_pk_fp8_f16 v168, v152, 1.0
	v_pk_fma_f16 v152, v152, v152, -2.0 op_sel:[0,1,1] op_sel_hi:[1,1,0]
	s_nop 0
	v_cvt_scalef32_pk_fp8_f16 v168, v152, 1.0 op_sel:[0,0,1]
	v_add_f32_e32 v152, v153, v153
	v_cvt_scalef32_pk_fp8_f16 v165, v157, 1.0 op_sel:[0,0,1]
	v_cvt_scalef32_pk_fp8_f16 v167, v155, 1.0 op_sel:[0,0,1]
	v_mfma_scale_f32_32x32x64_f8f6f4 v[32:47], v[170:177], v[136:143], v[32:47], v227, v226 op_sel_hi:[0,0,0]
	v_cvt_pk_f16_f32 v136, v154, v152
	v_cvt_scalef32_pk_fp8_f16 v169, v136, 1.0
	v_pk_fma_f16 v136, v136, v136, -2.0 op_sel:[1,0,1] op_sel_hi:[1,1,0]
	s_nop 0
	v_cvt_scalef32_pk_fp8_f16 v169, v136, 1.0 op_sel:[0,0,1]
	v_pk_fma_f16 v136, v136, v136, -2.0 op_sel:[0,1,1] op_sel_hi:[1,1,0]
	s_nop 0
	v_pk_fma_f16 v137, v136, v136, -2.0 op_sel:[0,1,1] op_sel_hi:[1,1,0]
	s_nop 0
	v_pk_fma_f16 v138, v137, v137, -2.0 op_sel:[0,1,1] op_sel_hi:[1,1,0]
	s_nop 0
	v_pk_fma_f16 v139, v138, v138, -2.0 op_sel:[0,1,1] op_sel_hi:[1,1,0]
	v_mfma_scale_f32_32x32x64_f8f6f4 v[48:63], v[170:177], v[144:151], v[48:63], v227, v226 op_sel_hi:[0,0,0]
	v_cvt_scalef32_pk_fp8_f16 v171, v138, 1.0
	v_cvt_scalef32_pk_fp8_f16 v170, v136, 1.0
	v_cvt_scalef32_pk_fp8_f16 v171, v139, 1.0 op_sel:[0,0,1]
	v_cvt_scalef32_pk_fp8_f16 v170, v137, 1.0 op_sel:[0,0,1]
	v_mfma_scale_f32_32x32x64_f8f6f4 v[16:31], v[236:243], v[144:151], v[16:31], v227, v226 op_sel_hi:[0,0,0]
	v_mul_f32_e32 v152, 0.15915494, v225
	ds_read_b128 v[136:139], v234 offset:32768
	ds_read_b128 v[140:143], v234 offset:33792
	v_cos_f32_e32 v153, v152
	v_sin_f32_e32 v152, v152
	v_mov_b32_e32 v205, v161
	s_waitcnt lgkmcnt(0)
	v_mfma_scale_f32_32x32x64_f8f6f4 v[96:111], v[136:143], v[128:135], v[96:111], v227, v226 op_sel_hi:[0,0,0]
	v_add_f32_e32 v153, v153, v153
	v_cvt_pk_f16_f32 v158, v152, v153
	v_mov_b32_e32 v203, v161
	v_cndmask_b32_e64 v162, 0, v222, s[0:1]
	v_mul_f32_e32 v163, 0.15915494, v223
	v_pk_fma_f16 v159, v158, v158, -2.0 op_sel:[1,0,1] op_sel_hi:[1,1,0]
	v_cndmask_b32_e64 v172, 0, v224, s[0:1]
	v_pk_fma_f16 v156, v159, v159, -2.0 op_sel:[0,1,1] op_sel_hi:[1,1,0]
	s_nop 0
	v_pk_fma_f16 v160, v156, v156, -2.0 op_sel:[0,1,1] op_sel_hi:[1,1,0]
	v_cvt_scalef32_pk_fp8_f16 v157, v156, 1.0
	v_cvt_scalef32_pk_fp8_f16 v156, v158, 1.0
	v_cvt_scalef32_pk_fp8_f16 v156, v159, 1.0 op_sel:[0,0,1]
	v_mfma_scale_f32_32x32x64_f8f6f4 v[112:127], v[136:143], v[164:171], v[112:127], v227, v226 op_sel_hi:[0,0,0]
	ds_read_b128 v[136:139], v234 offset:34816
	ds_read_b128 v[140:143], v234 offset:35840
	ds_read_b128 v[144:147], v234 offset:36864
	ds_read_b128 v[148:151], v234 offset:37888
	ds_read_b128 v[236:239], v234 offset:38912
	ds_read_b128 v[240:243], v234 offset:39936
	v_lshl_add_u64 v[152:153], v[204:205], 2, s[4:5]
	v_lshl_add_u64 v[154:155], v[202:203], 2, s[4:5]
	global_load_dword v225, v[152:153], off offset:48
	global_load_dword v222, v[154:155], off
	global_load_dword v224, v[154:155], off offset:3456
	global_load_dword v223, v[152:153], off offset:3504
	v_cvt_scalef32_pk_fp8_f16 v157, v160, 1.0 op_sel:[0,0,1]
	s_waitcnt lgkmcnt(4)
	v_mfma_scale_f32_32x32x64_f8f6f4 v[64:79], v[136:143], v[128:135], v[64:79], v227, v226 op_sel_hi:[0,0,0]
	v_mfma_scale_f32_32x32x64_f8f6f4 v[80:95], v[136:143], v[164:171], v[80:95], v227, v226 op_sel_hi:[0,0,0]
	v_mul_f32_e32 v136, v207, v208
	v_fma_f32 v137, v208, v208, -2.0
	v_cndmask_b32_e64 v138, v137, v136, s[0:1]
	v_mul_f32_e32 v136, v136, v137
	v_fma_f32 v137, v137, v137, -2.0
	v_cndmask_b32_e64 v139, v137, v136, s[0:1]
	v_cvt_pk_fp8_f32 v159, v138, v139
	v_mul_f32_e32 v136, v136, v137
	v_fma_f32 v137, v137, v137, -2.0
	v_cndmask_b32_e64 v136, v137, v136, s[0:1]
	v_cvt_pk_fp8_f32 v159, v136, v162 op_sel:[0,0,1]
	v_pk_fma_f16 v136, v160, v160, -2.0 op_sel:[0,1,1] op_sel_hi:[1,1,0]
	v_mov_b32_e32 v160, v161
	v_pk_fma_f16 v137, v136, v136, -2.0 op_sel:[0,1,1] op_sel_hi:[1,1,0]
	v_cvt_scalef32_pk_fp8_f16 v158, v136, 1.0
	v_cos_f32_e32 v136, v163
	v_cvt_scalef32_pk_fp8_f16 v158, v137, 1.0 op_sel:[0,0,1]
	v_sin_f32_e32 v137, v163
	s_waitcnt lgkmcnt(0)
	v_mfma_scale_f32_32x32x64_f8f6f4 v[0:15], v[236:243], v[128:135], v[0:15], v227, v226 op_sel_hi:[0,0,0]
	v_add_f32_e32 v136, v136, v136
	v_mov_b32_e32 v162, v161
	v_cvt_pk_f16_f32 v138, v137, v136
	v_pk_fma_f16 v139, v138, v138, -2.0 op_sel:[1,0,1] op_sel_hi:[1,1,0]
	s_nop 0
	v_pk_fma_f16 v136, v139, v139, -2.0 op_sel:[0,1,1] op_sel_hi:[1,1,0]
	v_mov_b32_e32 v163, v161
	v_pk_fma_f16 v140, v136, v136, -2.0 op_sel:[0,1,1] op_sel_hi:[1,1,0]
	v_cvt_scalef32_pk_fp8_f16 v137, v136, 1.0
	v_cvt_scalef32_pk_fp8_f16 v136, v138, 1.0
	v_cvt_scalef32_pk_fp8_f16 v136, v139, 1.0 op_sel:[0,0,1]
	v_mul_f32_e32 v138, v209, v210
	v_fma_f32 v139, v210, v210, -2.0
	v_cndmask_b32_e64 v141, v139, v138, s[0:1]
	v_mul_f32_e32 v138, v138, v139
	v_fma_f32 v142, v139, v139, -2.0
	v_cndmask_b32_e64 v143, v142, v138, s[0:1]
	v_cvt_pk_fp8_f32 v139, v141, v143
	v_mfma_scale_f32_32x32x64_f8f6f4 v[32:47], v[144:151], v[128:135], v[32:47], v227, v226 op_sel_hi:[0,0,0]
	v_mul_f32_e32 v128, v138, v142
	v_fma_f32 v129, v142, v142, -2.0
	v_cndmask_b32_e64 v128, v129, v128, s[0:1]
	v_cvt_pk_fp8_f32 v139, v128, v172 op_sel:[0,0,1]
	v_pk_fma_f16 v128, v140, v140, -2.0 op_sel:[0,1,1] op_sel_hi:[1,1,0]
	s_nop 0
	v_cvt_scalef32_pk_fp8_f16 v138, v128, 1.0
	v_pk_fma_f16 v128, v128, v128, -2.0 op_sel:[0,1,1] op_sel_hi:[1,1,0]
	v_cvt_scalef32_pk_fp8_f16 v137, v140, 1.0 op_sel:[0,0,1]
	v_cvt_scalef32_pk_fp8_f16 v138, v128, 1.0 op_sel:[0,0,1]
	v_mov_b32_e32 v140, v161
	v_mov_b32_e32 v141, v161
	v_mov_b32_e32 v142, v161
	v_mov_b32_e32 v143, v161
	v_mfma_scale_f32_32x32x64_f8f6f4 v[48:63], v[144:151], v[164:171], v[48:63], v227, v226 op_sel_hi:[0,0,0]
	v_mfma_scale_f32_32x32x64_f8f6f4 v[16:31], v[236:243], v[164:171], v[16:31], v227, v226 op_sel_hi:[0,0,0]
	ds_read_b128 v[128:131], v234 offset:40960
	ds_read_b128 v[132:135], v234 offset:41984
	s_waitcnt lgkmcnt(0)
	v_mfma_scale_f32_32x32x64_f8f6f4 v[96:111], v[128:135], v[156:163], v[96:111], v227, v226 op_sel_hi:[0,0,0]
	v_mfma_scale_f32_32x32x64_f8f6f4 v[112:127], v[128:135], v[136:143], v[112:127], v227, v226 op_sel_hi:[0,0,0]
	ds_read_b128 v[128:131], v234 offset:43008
	ds_read_b128 v[132:135], v234 offset:44032
	s_waitcnt lgkmcnt(0)
	v_mfma_scale_f32_32x32x64_f8f6f4 v[64:79], v[128:135], v[156:163], v[64:79], v227, v226 op_sel_hi:[0,0,0]
	v_mfma_scale_f32_32x32x64_f8f6f4 v[80:95], v[128:135], v[136:143], v[80:95], v227, v226 op_sel_hi:[0,0,0]
	ds_read_b128 v[128:131], v234 offset:45056
	ds_read_b128 v[132:135], v234 offset:46080
	s_waitcnt lgkmcnt(0)
	v_mfma_scale_f32_32x32x64_f8f6f4 v[32:47], v[128:135], v[156:163], v[32:47], v227, v226 op_sel_hi:[0,0,0]
	v_mfma_scale_f32_32x32x64_f8f6f4 v[48:63], v[128:135], v[136:143], v[48:63], v227, v226 op_sel_hi:[0,0,0]
	ds_read_b128 v[128:131], v234 offset:47104
	ds_read_b128 v[132:135], v234 offset:48128
	ds_read_b128 v[174:177], v234 offset:49152
	ds_read_b128 v[208:211], v234 offset:50176
	ds_read_b128 v[212:215], v234 offset:53248
	ds_read_b128 v[236:239], v234 offset:54272
	s_waitcnt lgkmcnt(4)
	v_mfma_scale_f32_32x32x64_f8f6f4 v[0:15], v[128:135], v[156:163], v[0:15], v227, v226 op_sel_hi:[0,0,0]
	v_mfma_scale_f32_32x32x64_f8f6f4 v[16:31], v[128:135], v[136:143], v[16:31], v227, v226 op_sel_hi:[0,0,0]
	v_cvt_pk_bf16_f32 v162, v96, v97 clamp
	v_cvt_pk_bf16_f32 v163, v98, v99 clamp
	v_cvt_pk_bf16_f32 v164, v100, v101 clamp
	v_cvt_pk_bf16_f32 v165, v102, v103 clamp
	v_cvt_pk_bf16_f32 v166, v112, v113 clamp
	v_cvt_pk_bf16_f32 v167, v114, v115 clamp
	v_cvt_pk_bf16_f32 v168, v116, v117 clamp
	v_cvt_pk_bf16_f32 v169, v118, v119 clamp
	v_cvt_pk_bf16_f32 v170, v104, v105 clamp
	v_cvt_pk_bf16_f32 v171, v106, v107 clamp
	v_cvt_pk_bf16_f32 v172, v108, v109 clamp
	v_add_u32_e32 v128, 0, v206
	v_cvt_pk_bf16_f32 v173, v110, v111 clamp
	v_add_u32_e32 v235, 0x18000, v128
	v_cvt_pk_bf16_f32 v202, v120, v121 clamp
	ds_read_b128 v[128:131], v235
	ds_read_b128 v[132:135], v235 offset:32
	ds_read_b128 v[136:139], v235 offset:64
	ds_read_b128 v[140:143], v235 offset:96
	v_cvt_pk_bf16_f32 v203, v122, v123 clamp
	ds_read_b128 v[96:99], v235 offset:128
	ds_read_b128 v[100:103], v235 offset:160
	ds_read_b128 v[104:107], v235 offset:192
	ds_read_b128 v[108:111], v235 offset:224
	v_cvt_pk_bf16_f32 v204, v124, v125 clamp
	v_cvt_pk_bf16_f32 v64, v64, v65
	s_waitcnt lgkmcnt(4)
	v_mfma_f32_32x32x16_bf16 v[144:159], v[174:177], v[166:169], v[128:143]
	v_cvt_pk_bf16_f32 v205, v126, v127 clamp
	ds_read_b128 v[240:243], v234 offset:57344
	ds_read_b128 v[244:247], v234 offset:58368
	ds_read_b128 v[248:251], v234 offset:61440
	ds_read_b128 v[252:255], v234 offset:62464
	v_cvt_pk_bf16_f32 v65, v74, v75 clamp
	v_cndmask_b32_e64 v230, v230, 0, s[14:15]
	v_mfma_f32_32x32x16_bf16 v[128:143], v[174:177], v[162:165], v[128:143]
	v_pk_max_i16 v174, v64, 0
	v_cvt_pk_bf16_f32 v175, v66, v67 clamp
	v_cvt_pk_bf16_f32 v176, v68, v69 clamp
	v_cvt_pk_bf16_f32 v177, v70, v71 clamp
	s_waitcnt lgkmcnt(4)
	v_mfma_f32_32x32x16_bf16 v[112:127], v[208:211], v[166:169], v[96:111]
	v_cvt_pk_bf16_f32 v80, v80, v81 clamp
	v_cvt_pk_bf16_f32 v81, v82, v83 clamp
	v_cvt_pk_bf16_f32 v82, v84, v85 clamp
	v_cvt_pk_bf16_f32 v83, v86, v87 clamp
	v_mfma_f32_32x32x16_bf16 v[96:111], v[208:211], v[162:165], v[96:111]
	v_cvt_pk_bf16_f32 v64, v72, v73 clamp
	v_cvt_pk_bf16_f32 v66, v76, v77 clamp
	v_cvt_pk_bf16_f32 v67, v78, v79 clamp
	v_cvt_pk_bf16_f32 v68, v88, v89 clamp
	v_cvt_pk_bf16_f32 v69, v90, v91 clamp
	v_cvt_pk_bf16_f32 v70, v92, v93 clamp
	v_cvt_pk_bf16_f32 v71, v94, v95 clamp
	v_add_u32_e32 v160, 0x14000, v234
	v_mfma_f32_32x32x16_bf16 v[128:143], v[212:215], v[170:173], v[128:143]
	v_mfma_f32_32x32x16_bf16 v[144:159], v[212:215], v[202:205], v[144:159]
	v_mfma_f32_32x32x16_bf16 v[96:111], v[236:239], v[170:173], v[96:111]
	v_mfma_f32_32x32x16_bf16 v[112:127], v[236:239], v[202:205], v[112:127]
	v_cvt_pk_bf16_f32 v76, v32, v33 clamp
	v_cvt_pk_bf16_f32 v77, v34, v35 clamp
	v_cvt_pk_bf16_f32 v78, v36, v37 clamp
	v_cvt_pk_bf16_f32 v79, v38, v39 clamp
	v_cvt_pk_bf16_f32 v88, v48, v49 clamp
	v_cvt_pk_bf16_f32 v89, v50, v51 clamp
	v_cvt_pk_bf16_f32 v90, v52, v53 clamp
	v_cvt_pk_bf16_f32 v91, v54, v55 clamp
	s_waitcnt lgkmcnt(3)
	v_mfma_f32_32x32x16_bf16 v[128:143], v[240:243], v[174:177], v[128:143]
	v_cvt_pk_bf16_f32 v72, v40, v41 clamp
	v_cvt_pk_bf16_f32 v73, v42, v43 clamp
	v_cvt_pk_bf16_f32 v74, v44, v45 clamp
	v_mfma_f32_32x32x16_bf16 v[144:159], v[240:243], v[80:83], v[144:159]
	ds_read_b128 v[92:95], v233 offset:16384
	ds_read_b128 v[208:211], v233 offset:17408
	ds_read_b128 v[236:239], v233 offset:20480
	ds_read_b128 v[240:243], v233 offset:21504
	v_cvt_pk_bf16_f32 v75, v46, v47 clamp
	v_cvt_pk_bf16_f32 v84, v56, v57 clamp
	v_cvt_pk_bf16_f32 v85, v58, v59 clamp
	s_waitcnt lgkmcnt(6)
	v_mfma_f32_32x32x16_bf16 v[96:111], v[244:247], v[174:177], v[96:111]
	v_cvt_pk_bf16_f32 v86, v60, v61 clamp
	v_cvt_pk_bf16_f32 v87, v62, v63 clamp
	v_mfma_f32_32x32x16_bf16 v[112:127], v[244:247], v[80:83], v[112:127]
	s_waitcnt lgkmcnt(5)
	v_mfma_f32_32x32x16_bf16 v[128:143], v[248:251], v[64:67], v[128:143]
	v_mfma_f32_32x32x16_bf16 v[144:159], v[248:251], v[68:71], v[144:159]
	s_waitcnt lgkmcnt(4)
	v_mfma_f32_32x32x16_bf16 v[96:111], v[252:255], v[64:67], v[96:111]
	v_mfma_f32_32x32x16_bf16 v[112:127], v[252:255], v[68:71], v[112:127]
	v_cvt_pk_bf16_f32 v206, v0, v1 clamp
	v_cvt_pk_bf16_f32 v207, v2, v3 clamp
	v_cvt_pk_bf16_f32 v0, v4, v5
	s_waitcnt lgkmcnt(2)
	v_mfma_f32_32x32x16_bf16 v[96:111], v[208:211], v[76:79], v[96:111]
	ds_read_b128 v[32:35], v233 offset:24576
	ds_read_b128 v[36:39], v233 offset:25600
	ds_read_b128 v[40:43], v233 offset:28672
	ds_read_b128 v[44:47], v233 offset:29696
	v_mfma_f32_32x32x16_bf16 v[112:127], v[208:211], v[88:91], v[112:127]
	v_pk_max_i16 v208, v0, 0
	v_cvt_pk_bf16_f32 v209, v6, v7 clamp
	v_cvt_pk_bf16_f32 v214, v16, v17 clamp
	v_cvt_pk_bf16_f32 v215, v18, v19 clamp
	v_cvt_pk_bf16_f32 v216, v20, v21 clamp
	v_cvt_pk_bf16_f32 v217, v22, v23 clamp
	v_mfma_f32_32x32x16_bf16 v[128:143], v[92:95], v[76:79], v[128:143]
	v_cvt_pk_bf16_f32 v0, v8, v9
	v_mfma_f32_32x32x16_bf16 v[144:159], v[92:95], v[88:91], v[144:159]
	v_pk_max_i16 v92, v0, 0
	v_cvt_pk_bf16_f32 v93, v10, v11 clamp
	v_cvt_pk_bf16_f32 v94, v12, v13 clamp
	v_cvt_pk_bf16_f32 v95, v14, v15 clamp
	v_cvt_pk_bf16_f32 v210, v24, v25 clamp
	v_cvt_pk_bf16_f32 v211, v26, v27 clamp
	v_cvt_pk_bf16_f32 v212, v28, v29 clamp
	v_cvt_pk_bf16_f32 v213, v30, v31 clamp
	s_waitcnt lgkmcnt(5)
	v_mfma_f32_32x32x16_bf16 v[128:143], v[236:239], v[72:75], v[128:143]
	v_mfma_f32_32x32x16_bf16 v[144:159], v[236:239], v[84:87], v[144:159]
	s_waitcnt lgkmcnt(4)
	v_mfma_f32_32x32x16_bf16 v[96:111], v[240:243], v[72:75], v[96:111]
	v_mfma_f32_32x32x16_bf16 v[112:127], v[240:243], v[84:87], v[112:127]
	s_waitcnt lgkmcnt(3)
	v_mfma_f32_32x32x16_bf16 v[128:143], v[32:35], v[206:209], v[128:143]
	ds_read_b128 v[0:3], v234 offset:51200
	ds_read_b128 v[236:239], v234 offset:52224
	ds_read_b128 v[240:243], v234 offset:55296
	ds_read_b128 v[244:247], v234 offset:56320
	v_mfma_f32_32x32x16_bf16 v[144:159], v[32:35], v[214:217], v[144:159]
	s_waitcnt lgkmcnt(6)
	v_mfma_f32_32x32x16_bf16 v[96:111], v[36:39], v[206:209], v[96:111]
	v_mfma_f32_32x32x16_bf16 v[112:127], v[36:39], v[214:217], v[112:127]
	s_waitcnt lgkmcnt(5)
	v_mfma_f32_32x32x16_bf16 v[128:143], v[40:43], v[92:95], v[128:143]
	v_mfma_f32_32x32x16_bf16 v[144:159], v[40:43], v[210:213], v[144:159]
	s_waitcnt lgkmcnt(4)
	v_mfma_f32_32x32x16_bf16 v[96:111], v[44:47], v[92:95], v[96:111]
	v_mfma_f32_32x32x16_bf16 v[112:127], v[44:47], v[210:213], v[112:127]
	ds_read_b128 v[32:35], v235 offset:256
	ds_read_b128 v[36:39], v235 offset:288
	ds_read_b128 v[40:43], v235 offset:320
	ds_read_b128 v[44:47], v235 offset:352
	s_nop 3
	v_cvt_pk_bf16_f32 v128, v128, v129 clamp
	v_cvt_pk_bf16_f32 v129, v130, v131 clamp
	v_cvt_pk_bf16_f32 v130, v132, v133 clamp
	v_cvt_pk_bf16_f32 v131, v134, v135 clamp
	s_waitcnt lgkmcnt(0)
	v_mfma_f32_32x32x16_bf16 v[48:63], v[0:3], v[166:169], v[32:47]
	v_cvt_pk_bf16_f32 v132, v144, v145 clamp
	v_cvt_pk_bf16_f32 v133, v146, v147 clamp
	v_cvt_pk_bf16_f32 v134, v148, v149 clamp
	v_cvt_pk_bf16_f32 v135, v150, v151 clamp
	v_mfma_f32_32x32x16_bf16 v[32:47], v[0:3], v[162:165], v[32:47]
	ds_read_b128 v[0:3], v235 offset:384
	ds_read_b128 v[4:7], v235 offset:416
	ds_read_b128 v[8:11], v235 offset:448
	ds_read_b128 v[12:15], v235 offset:480
	s_waitcnt lgkmcnt(0)
	v_mfma_f32_32x32x16_bf16 v[16:31], v[236:239], v[166:169], v[0:15]
	v_mfma_f32_32x32x16_bf16 v[0:15], v[236:239], v[162:165], v[0:15]
	ds_read_b128 v[162:165], v234 offset:59392
	ds_read_b128 v[166:169], v234 offset:60416
	ds_read_b128 v[236:239], v234 offset:63488
	ds_read_b128 v[248:251], v234 offset:64512
	v_mfma_f32_32x32x16_bf16 v[0:15], v[244:247], v[170:173], v[0:15]
	v_mfma_f32_32x32x16_bf16 v[32:47], v[240:243], v[170:173], v[32:47]
	v_mfma_f32_32x32x16_bf16 v[48:63], v[240:243], v[202:205], v[48:63]
	v_mfma_f32_32x32x16_bf16 v[16:31], v[244:247], v[202:205], v[16:31]
	s_waitcnt lgkmcnt(2)
	v_mfma_f32_32x32x16_bf16 v[0:15], v[166:169], v[174:177], v[0:15]
	v_cvt_pk_bf16_f32 v136, v136, v137 clamp
	v_cvt_pk_bf16_f32 v137, v138, v139 clamp
	v_cvt_pk_bf16_f32 v138, v140, v141 clamp
	v_cvt_pk_bf16_f32 v139, v142, v143 clamp
	v_cvt_pk_bf16_f32 v140, v152, v153 clamp
	v_mfma_f32_32x32x16_bf16 v[32:47], v[162:165], v[174:177], v[32:47]
	v_mfma_f32_32x32x16_bf16 v[48:63], v[162:165], v[80:83], v[48:63]
	v_mfma_f32_32x32x16_bf16 v[16:31], v[166:169], v[80:83], v[16:31]
	ds_read_b128 v[80:83], v233 offset:18432
	ds_read_b128 v[144:147], v233 offset:19456
	ds_read_b128 v[148:151], v233 offset:22528
	ds_read_b128 v[162:165], v233 offset:23552
	s_waitcnt lgkmcnt(4)
	v_mfma_f32_32x32x16_bf16 v[0:15], v[248:251], v[64:67], v[0:15]
	v_mfma_f32_32x32x16_bf16 v[32:47], v[236:239], v[64:67], v[32:47]
	v_cvt_pk_bf16_f32 v141, v154, v155 clamp
	v_cvt_pk_bf16_f32 v142, v156, v157 clamp
	v_cvt_pk_bf16_f32 v143, v158, v159 clamp
	v_mfma_f32_32x32x16_bf16 v[48:63], v[236:239], v[68:71], v[48:63]
	v_mfma_f32_32x32x16_bf16 v[16:31], v[248:251], v[68:71], v[16:31]
	s_waitcnt lgkmcnt(2)
	v_mfma_f32_32x32x16_bf16 v[0:15], v[144:147], v[76:79], v[0:15]
	v_mfma_f32_32x32x16_bf16 v[32:47], v[80:83], v[76:79], v[32:47]
	v_mfma_f32_32x32x16_bf16 v[48:63], v[80:83], v[88:91], v[48:63]
	ds_read_b128 v[64:67], v233 offset:26624
	ds_read_b128 v[68:71], v233 offset:27648
	ds_read_b128 v[76:79], v233 offset:30720
	ds_read_b128 v[80:83], v233 offset:31744
	v_mfma_f32_32x32x16_bf16 v[16:31], v[144:147], v[88:91], v[16:31]
	v_cvt_pk_bf16_f32 v96, v96, v97 clamp
	v_cvt_pk_bf16_f32 v97, v98, v99 clamp
	v_cvt_pk_bf16_f32 v98, v100, v101 clamp
	v_cvt_pk_bf16_f32 v99, v102, v103 clamp
	s_waitcnt lgkmcnt(4)
	v_mfma_f32_32x32x16_bf16 v[0:15], v[162:165], v[72:75], v[0:15]
	v_cvt_pk_bf16_f32 v100, v112, v113 clamp
	v_mfma_f32_32x32x16_bf16 v[32:47], v[148:151], v[72:75], v[32:47]
	v_cvt_pk_bf16_f32 v101, v114, v115 clamp
	v_cvt_pk_bf16_f32 v102, v116, v117 clamp
	v_cvt_pk_bf16_f32 v103, v118, v119 clamp
	v_mfma_f32_32x32x16_bf16 v[48:63], v[148:151], v[84:87], v[48:63]
	v_mfma_f32_32x32x16_bf16 v[16:31], v[162:165], v[84:87], v[16:31]
	s_waitcnt lgkmcnt(2)
	v_mfma_f32_32x32x16_bf16 v[0:15], v[68:71], v[206:209], v[0:15]
	ds_read_b128 v[84:87], v160
	ds_read_b128 v[112:115], v160 offset:1024
	ds_read_b128 v[116:119], v160 offset:2048
	ds_read_b128 v[144:147], v160 offset:3072
	v_mfma_f32_32x32x16_bf16 v[32:47], v[64:67], v[206:209], v[32:47]
	v_mfma_f32_32x32x16_bf16 v[48:63], v[64:67], v[214:217], v[48:63]
	v_cvt_pk_bf16_f32 v104, v104, v105 clamp
	v_cvt_pk_bf16_f32 v105, v106, v107 clamp
	v_cvt_pk_bf16_f32 v106, v108, v109 clamp
	v_cvt_pk_bf16_f32 v107, v110, v111 clamp
	v_mfma_f32_32x32x16_bf16 v[16:31], v[68:71], v[214:217], v[16:31]
	v_cvt_pk_bf16_f32 v108, v120, v121 clamp
	v_cvt_pk_bf16_f32 v109, v122, v123 clamp
	v_cvt_pk_bf16_f32 v110, v124, v125 clamp
	s_waitcnt lgkmcnt(4)
	v_mfma_f32_32x32x16_bf16 v[0:15], v[80:83], v[92:95], v[0:15]
	v_cvt_pk_bf16_f32 v111, v126, v127 clamp
	v_mfma_f32_32x32x16_bf16 v[32:47], v[76:79], v[92:95], v[32:47]
	v_mfma_f32_32x32x16_bf16 v[48:63], v[76:79], v[210:213], v[48:63]
	v_mfma_f32_32x32x16_bf16 v[16:31], v[80:83], v[210:213], v[16:31]
	s_waitcnt lgkmcnt(3)
	v_mfma_f32_4x4x4_16b_bf16 v[64:67], v[84:85], v[128:129], 0
	v_mfma_f32_4x4x4_16b_bf16 v[68:71], v[86:87], v[130:131], 0
	s_nop 7
	v_cvt_pk_bf16_f32 v32, v32, v33 clamp
	v_cvt_pk_bf16_f32 v33, v34, v35 clamp
	v_cvt_pk_bf16_f32 v34, v36, v37 clamp
	v_cvt_pk_bf16_f32 v35, v38, v39 clamp
	v_mfma_f32_4x4x4_16b_bf16 v[80:83], v[84:85], v[132:133], 0
	v_mfma_f32_4x4x4_16b_bf16 v[88:91], v[86:87], v[134:135], 0
	v_cvt_pk_bf16_f32 v48, v48, v49 clamp
	v_cvt_pk_bf16_f32 v49, v50, v51 clamp
	v_cvt_pk_bf16_f32 v50, v52, v53 clamp
	v_cvt_pk_bf16_f32 v51, v54, v55 clamp
	s_waitcnt lgkmcnt(2)
	v_mfma_f32_4x4x4_16b_bf16 v[64:67], v[112:113], v[136:137], v[64:67]
	v_mfma_f32_4x4x4_16b_bf16 v[68:71], v[114:115], v[138:139], v[68:71]
	v_cvt_pk_bf16_f32 v40, v40, v41 clamp
	v_cvt_pk_bf16_f32 v41, v42, v43 clamp
	v_cvt_pk_bf16_f32 v42, v44, v45 clamp
	v_cvt_pk_bf16_f32 v43, v46, v47 clamp
	v_mfma_f32_4x4x4_16b_bf16 v[80:83], v[112:113], v[140:141], v[80:83]
	v_mfma_f32_4x4x4_16b_bf16 v[88:91], v[114:115], v[142:143], v[88:91]
	v_cvt_pk_bf16_f32 v52, v56, v57
	v_cvt_pk_bf16_f32 v53, v58, v59
	v_cvt_pk_bf16_f32 v54, v60, v61
	v_cvt_pk_bf16_f32 v55, v62, v63
	s_waitcnt lgkmcnt(1)
	v_mfma_f32_4x4x4_16b_bf16 v[64:67], v[116:117], v[96:97], v[64:67]
	v_mfma_f32_4x4x4_16b_bf16 v[68:71], v[118:119], v[98:99], v[68:71]
	ds_read_b128 v[36:39], v160 offset:4096
	ds_read_b128 v[96:99], v160 offset:5120
	v_cvt_pk_bf16_f32 v0, v0, v1 clamp
	v_cvt_pk_bf16_f32 v1, v2, v3 clamp
	v_cvt_pk_bf16_f32 v2, v4, v5 clamp
	v_cvt_pk_bf16_f32 v3, v6, v7 clamp
	v_mfma_f32_4x4x4_16b_bf16 v[80:83], v[116:117], v[100:101], v[80:83]
	v_mfma_f32_4x4x4_16b_bf16 v[88:91], v[118:119], v[102:103], v[88:91]
	ds_read_b128 v[4:7], v160 offset:7168
	v_cvt_pk_bf16_f32 v12, v12, v13
	v_cvt_pk_bf16_f32 v13, v14, v15
	v_cvt_pk_bf16_f32 v24, v24, v25
	v_cvt_pk_bf16_f32 v25, v26, v27
	s_waitcnt lgkmcnt(3)
	v_mfma_f32_4x4x4_16b_bf16 v[64:67], v[144:145], v[104:105], v[64:67]
	v_mfma_f32_4x4x4_16b_bf16 v[68:71], v[146:147], v[106:107], v[68:71]
	v_cvt_pk_bf16_f32 v26, v28, v29
	v_cvt_pk_bf16_f32 v27, v30, v31
	v_cndmask_b32_e64 v219, v219, 0, s[14:15]
	v_cndmask_b32_e64 v218, v218, 0, s[14:15]
	v_mfma_f32_4x4x4_16b_bf16 v[80:83], v[144:145], v[108:109], v[80:83]
	v_mfma_f32_4x4x4_16b_bf16 v[88:91], v[146:147], v[110:111], v[88:91]
	s_waitcnt lgkmcnt(2)
	v_mfma_f32_4x4x4_16b_bf16 v[64:67], v[36:37], v[32:33], v[64:67]
	v_mfma_f32_4x4x4_16b_bf16 v[68:71], v[38:39], v[34:35], v[68:71]
	v_cvt_pk_bf16_f32 v34, v20, v21
	v_cvt_pk_bf16_f32 v35, v22, v23
	ds_read_b128 v[20:23], v160 offset:6144
	v_cvt_pk_bf16_f32 v32, v16, v17
	v_cvt_pk_bf16_f32 v33, v18, v19
	v_pk_max_i16 v16, v52, 0
	v_pk_max_i16 v17, v53, 0
	v_mfma_f32_4x4x4_16b_bf16 v[80:83], v[36:37], v[48:49], v[80:83]
	v_mfma_f32_4x4x4_16b_bf16 v[88:91], v[38:39], v[50:51], v[88:91]
	v_pk_max_i16 v18, v54, 0
	v_pk_max_i16 v19, v55, 0
	s_waitcnt lgkmcnt(2)
	v_mfma_f32_4x4x4_16b_bf16 v[64:67], v[96:97], v[40:41], v[64:67]
	v_mfma_f32_4x4x4_16b_bf16 v[68:71], v[98:99], v[42:43], v[68:71]
	v_mfma_f32_4x4x4_16b_bf16 v[80:83], v[96:97], v[16:17], v[80:83]
	v_mfma_f32_4x4x4_16b_bf16 v[88:91], v[98:99], v[18:19], v[88:91]
	v_cvt_pk_bf16_f32 v16, v8, v9
	v_cvt_pk_bf16_f32 v17, v10, v11
	v_pk_max_i16 v8, v24, 0
	v_pk_max_i16 v9, v25, 0
	v_pk_max_i16 v10, v26, 0
	v_pk_max_i16 v11, v27, 0
	s_waitcnt lgkmcnt(0)
	v_mfma_f32_4x4x4_16b_bf16 v[64:67], v[20:21], v[0:1], v[64:67]
	v_mfma_f32_4x4x4_16b_bf16 v[68:71], v[22:23], v[2:3], v[68:71]
	v_pk_max_i16 v0, v32, 0
	v_pk_max_i16 v1, v33, 0
	v_pk_max_i16 v2, v34, 0
	v_pk_max_i16 v3, v35, 0
	s_nop 1
	v_mfma_f32_4x4x4_16b_bf16 v[80:83], v[20:21], v[0:1], v[80:83]
	v_mfma_f32_4x4x4_16b_bf16 v[88:91], v[22:23], v[2:3], v[88:91]
	v_pk_max_i16 v0, v16, 0
	v_pk_max_i16 v1, v17, 0
	v_pk_max_i16 v2, v12, 0
	v_pk_max_i16 v3, v13, 0
	s_nop 1
	v_mfma_f32_4x4x4_16b_bf16 v[64:67], v[4:5], v[0:1], v[64:67]
	v_mfma_f32_4x4x4_16b_bf16 v[68:71], v[6:7], v[2:3], v[68:71]
	v_mfma_f32_4x4x4_16b_bf16 v[80:83], v[4:5], v[8:9], v[80:83]
	v_mfma_f32_4x4x4_16b_bf16 v[88:91], v[6:7], v[10:11], v[88:91]
	s_waitcnt vmcnt(10)
	s_nop 3
	v_pk_add_f32 v[64:65], v[64:65], v[68:69]
	v_pk_add_f32 v[80:81], v[80:81], v[88:89]
	v_add_f32_e32 v66, v66, v70
	v_add_f32_e32 v82, v82, v90
	s_nop 1
	v_permlane32_swap_b32_e32 v64, v80
	v_permlane32_swap_b32_e32 v65, v81
	v_permlane32_swap_b32_e32 v66, v82
	s_nop 0
	v_add_f32_e32 v64, v64, v80
	v_add_f32_e32 v65, v65, v81
	v_add_f32_e32 v66, v66, v82
	v_add_f32_e32 v3, s10, v64
	v_add_f32_e32 v4, s11, v65
	v_add_f32_e32 v5, s18, v66
	v_mul_f32_e32 v3, 0xbfb8aa3b, v3
	v_mul_f32_e32 v4, 0xbfb8aa3b, v4
	v_mul_f32_e32 v5, 0xbfb8aa3b, v5
	v_exp_f32_e32 v3, v3
	v_exp_f32_e32 v4, v4
	v_exp_f32_e32 v5, v5
	v_add_f32_e32 v3, 1.0, v3
	v_add_f32_e32 v4, 1.0, v4
	v_add_f32_e32 v5, 1.0, v5
	v_rcp_f32_e32 v3, v3
	v_rcp_f32_e32 v4, v4
	v_rcp_f32_e32 v5, v5
	v_fmac_f32_e32 v218, v232, v3
	v_fmac_f32_e32 v219, v232, v4
	v_fmac_f32_e32 v230, v232, v5
	s_andn2_b64 vcc, exec, s[12:13]
	s_cbranch_vccnz .LBB1_6
	v_and_b32_e32 v1, 64, v229
	v_xor_b32_e32 v0, 32, v229
	v_add_u32_e32 v2, 64, v1
	v_cmp_lt_i32_e32 vcc, v0, v2
	s_nop 1
	v_cndmask_b32_e32 v0, v229, v0, vcc
	v_lshlrev_b32_e32 v0, 2, v0
	s_waitcnt lgkmcnt(0)
	ds_bpermute_b32 v1, v0, v230
	v_xor_b32_e32 v3, 16, v229
	v_cmp_lt_i32_e32 vcc, v3, v2
	ds_bpermute_b32 v4, v0, v218
	ds_bpermute_b32 v5, v0, v219
	v_cndmask_b32_e32 v3, v229, v3, vcc
	v_lshlrev_b32_e32 v3, 2, v3
	s_waitcnt lgkmcnt(2)
	v_add_f32_e32 v1, v230, v1
	ds_bpermute_b32 v6, v3, v1
	v_xor_b32_e32 v0, 8, v229
	v_cmp_lt_i32_e32 vcc, v0, v2
	v_xor_b32_e32 v9, 4, v229
	s_waitcnt lgkmcnt(0)
	v_add_f32_e32 v6, v1, v6
	v_cndmask_b32_e32 v0, v229, v0, vcc
	v_lshlrev_b32_e32 v7, 2, v0
	v_pk_add_f32 v[0:1], v[218:219], v[4:5]
	ds_bpermute_b32 v4, v3, v0
	ds_bpermute_b32 v5, v3, v1
	ds_bpermute_b32 v8, v7, v6
	v_cmp_lt_i32_e32 vcc, v9, v2
	s_waitcnt lgkmcnt(1)
	v_pk_add_f32 v[0:1], v[0:1], v[4:5]
	ds_bpermute_b32 v4, v7, v0
	ds_bpermute_b32 v5, v7, v1
	v_cndmask_b32_e32 v3, v229, v9, vcc
	s_waitcnt lgkmcnt(2)
	v_add_f32_e32 v6, v6, v8
	v_lshlrev_b32_e32 v3, 2, v3
	ds_bpermute_b32 v8, v3, v6
	s_waitcnt lgkmcnt(1)
	v_pk_add_f32 v[0:1], v[0:1], v[4:5]
	ds_bpermute_b32 v4, v3, v0
	ds_bpermute_b32 v5, v3, v1
	v_xor_b32_e32 v3, 2, v229
	v_cmp_lt_i32_e32 vcc, v3, v2
	s_waitcnt lgkmcnt(2)
	v_add_f32_e32 v6, v6, v8
	s_waitcnt lgkmcnt(0)
	v_pk_add_f32 v[0:1], v[0:1], v[4:5]
	v_cndmask_b32_e32 v3, v229, v3, vcc
	v_lshlrev_b32_e32 v3, 2, v3
	ds_bpermute_b32 v4, v3, v0
	ds_bpermute_b32 v5, v3, v1
	ds_bpermute_b32 v3, v3, v6
	s_waitcnt lgkmcnt(1)
	v_pk_add_f32 v[0:1], v[0:1], v[4:5]
	s_waitcnt lgkmcnt(0)
	v_add_f32_e32 v4, v6, v3
	v_xor_b32_e32 v3, 1, v229
	v_cmp_lt_i32_e32 vcc, v3, v2
	s_nop 1
	v_cndmask_b32_e32 v2, v229, v3, vcc
	v_lshlrev_b32_e32 v5, 2, v2
	ds_bpermute_b32 v2, v5, v0
	ds_bpermute_b32 v3, v5, v1
	ds_bpermute_b32 v5, v5, v4
	s_and_saveexec_b64 s[12:13], s[2:3]
	s_cbranch_execz .LBB1_5
	v_lshl_add_u32 v6, v231, 1, v231
	v_ashrrev_i32_e32 v7, 31, v6
	s_waitcnt lgkmcnt(0)
	v_add_f32_e32 v4, v4, v5
	v_lshl_add_u64 v[6:7], v[6:7], 2, s[8:9]
	v_pk_add_f32 v[2:3], v[0:1], v[2:3]
	global_store_dwordx3 v[6:7], v[2:4], off
	s_branch .LBB1_5
